# T3a stage D: transposed operand images written via in-register 8x8 lane transpose (dpp/perm/permlane swaps) + 4 ds_write_b128 instead of 32 bank-conflicted ds_write_b16
# speedup vs baseline: 1.0248x; 1.0248x over previous
; __device__ __forceinline__ void phase1(const int WID_, const In& I, char* lds) {
;     ...
;                 float x = ex(wr[w_]); r_[e] = x + (ex(pr[w_]) - x) * mur[e];
;                 x = ex(wk[w_]); const float k = x + (ex(pk[w_]) - x) * muk[e];
;                 x = ex(wv4[w_]); v_[e] = x + (ex(pv[w_]) - x) * muv[e];
;                 a_[e] = ex(wa[w_]); kk_[e] = k * ckk[e]; ss += kk_[e] * kk_[e];
;                 kp_[e] = k * (1.f + (a_[e] - 1.f) * cka[e]); rk += r_[e] * kp_[e] * crk[e];
;                 G[s * 64 + cg * 8 + e] = ex(wl[w_]); }
;             ss += dpp16<0xB1>(ss); ss += dpp16<0x4E>(ss); ss += dpp16<0x141>(ss);
;             const float inv = 1.f / fmaxf(sqrtf(ss), 1e-12f);
; #pragma unroll
;             for (int e = 0; e < 8; ++e) { kk_[e] *= inv; b_[e] = kk_[e] * a_[e]; }
;             rk += dpp16<0xB1>(rk); rk += dpp16<0x4E>(rk); rk += dpp16<0x141>(rk);
;             if (cg == 0) I.RK[m * 8 + h] = rk;
;         }
;         CK_BAR();
;         { const int ch = tid & 63, part = tid >> 6; float run = 0.f;
; #pragma unroll
;           for (int i = 0; i < 8; ++i) { run += G[(8 * part + i) * 64 + ch]; G[(8 * part + i) * 64 + ch] = run; }
;           TOT[part * 64 + ch] = run; }
;         CK_BAR();
;         { const int ch = tid & 63, part = tid >> 6; float off = 0.f;
;           for (int p = 0; p < part; ++p) off += TOT[p * 64 + ch];
; #pragma unroll
;           for (int i = 0; i < 8; ++i) G[(8 * part + i) * 64 + ch] += off; }
;         CK_BAR();
;         float glast[8];
;         {
;             unsigned pab[4], prb[4], pbb[4], pkb[4];
;             float ab[8], rb[8], bb[8], kb[8], bt[8], kt[8];
;             const float4 g0_ = *(const float4*)(G + s * 64 + cg * 8), g1_ = *(const float4*)(G + s * 64 + cg * 8 + 4);
;             const int sm = (s > 0) ? s - 1 : 0; const float msk = (s > 0) ? 1.f : 0.f;
;             const float4 m0_ = *(const float4*)(G + sm * 64 + cg * 8), m1_ = *(const float4*)(G + sm * 64 + cg * 8 + 4);
;             const float4 l0_ = *(const float4*)(G + 63 * 64 + cg * 8), l1_ = *(const float4*)(G + 63 * 64 + cg * 8 + 4);
;             const float gv_[8] = {g0_.x, g0_.y, g0_.z, g0_.w, g1_.x, g1_.y, g1_.z, g1_.w}, mv_[8] = {m0_.x, m0_.y, m0_.z, m0_.w, m1_.x, m1_.y, m1_.z, m1_.w}, lv_[8] = {l0_.x, l0_.y, l0_.z, l0_.w, l1_.x, l1_.y, l1_.z, l1_.w};
; #pragma unroll
.Lscan_done:
	s_waitcnt lgkmcnt(0)
	v_cndmask_b32_e32 v6, 0, v24, vcc
	v_cndmask_b32_e32 v7, 0, v26, vcc
	v_cndmask_b32_e32 v24, 0, v25, vcc
	v_cndmask_b32_e32 v25, 0, v27, vcc
	v_lshlrev_b32_e32 v26, 16, v20
	v_lshlrev_b32_e32 v27, 16, v6
	v_and_b32_e32 v20, 0xffff0000, v20
	v_and_b32_e32 v6, 0xffff0000, v6
	v_sub_f32_e32 v27, v27, v26
	v_sub_f32_e32 v6, v6, v20
	v_fma_mix_f32 v53, v27, v0, v26 op_sel_hi:[0,1,0]
	v_fma_mix_f32 v68, v6, v0, v20 op_sel:[0,1,0] op_sel_hi:[0,1,0]
	v_lshlrev_b32_e32 v0, 16, v21
	v_lshlrev_b32_e32 v6, 16, v24
	v_sub_f32_e32 v6, v6, v0
	v_fma_mix_f32 v72, v6, v1, v0 op_sel_hi:[0,1,0]
	v_and_b32_e32 v0, 0xffff0000, v21
	v_and_b32_e32 v6, 0xffff0000, v24
	v_sub_f32_e32 v6, v6, v0
	v_fma_mix_f32 v73, v6, v1, v0 op_sel:[0,1,0] op_sel_hi:[0,1,0]
	v_lshlrev_b32_e32 v0, 16, v22
	v_lshlrev_b32_e32 v1, 16, v7
	v_sub_f32_e32 v1, v1, v0
	v_fma_mix_f32 v74, v1, v2, v0 op_sel_hi:[0,1,0]
	v_and_b32_e32 v0, 0xffff0000, v22
	v_and_b32_e32 v1, 0xffff0000, v7
	v_sub_f32_e32 v1, v1, v0
	v_fma_mix_f32 v75, v1, v2, v0 op_sel:[0,1,0] op_sel_hi:[0,1,0]
	v_add_f32_e32 v2, v56, v57
	s_mov_b32 s0, 0xf800000
	v_mul_f32_e32 v6, 0x4f800000, v2
	v_cmp_gt_f32_e32 vcc, s0, v2
	v_lshlrev_b32_e32 v0, 16, v23
	v_lshlrev_b32_e32 v1, 16, v25
	v_cndmask_b32_e32 v2, v2, v6, vcc
	v_sqrt_f32_e32 v6, v2
	v_sub_f32_e32 v1, v1, v0
	v_fma_mix_f32 v78, v1, v3, v0 op_sel_hi:[0,1,0]
	v_and_b32_e32 v0, 0xffff0000, v23
	v_add_u32_e32 v1, -1, v6
	v_fma_f32 v7, -v1, v6, v2
	v_cmp_ge_f32_e64 s[0:1], 0, v7
	v_add_u32_e32 v7, 1, v6
	v_lshlrev_b32_e32 v52, 3, v61
	v_cndmask_b32_e64 v1, v6, v1, s[0:1]
	v_fma_f32 v6, -v7, v6, v2
	v_cmp_lt_f32_e64 s[0:1], 0, v6
	s_add_i32 s33, s40, s94
	s_nop 0
	v_cndmask_b32_e64 v1, v1, v7, s[0:1]
	v_mul_f32_e32 v6, 0x37800000, v1
	v_cndmask_b32_e32 v1, v1, v6, vcc
	v_cmp_class_f32_e32 vcc, v2, v77
	v_and_b32_e32 v7, 0xffff0000, v25
	v_sub_f32_e32 v7, v7, v0
	v_cndmask_b32_e32 v1, v1, v2, vcc
	v_max_f32_e32 v1, 0x2b8cbccc, v1
	v_div_scale_f32 v2, s[0:1], v1, v1, 1.0
	v_rcp_f32_e32 v6, v2
	v_fma_mix_f32 v79, v7, v3, v0 op_sel:[0,1,0] op_sel_hi:[0,1,0]
	s_movk_i32 s0, 0xff00
	s_min_i32 s1, s33, 0x1fff
	v_fma_f32 v0, -v2, v6, 1.0
	v_fmac_f32_e32 v6, v0, v6
	v_div_scale_f32 v0, vcc, 1.0, v1, 1.0
	v_mul_f32_e32 v3, v0, v6
	v_fma_f32 v7, -v2, v3, v0
	v_fmac_f32_e32 v3, v7, v6
	v_fma_f32 v0, -v2, v3, v0
	v_div_fmas_f32 v0, v0, v6, v3
	v_div_fixup_f32 v0, v0, v1, 1.0
	v_pk_mul_f32 v[54:55], v[8:9], v[0:1] op_sel_hi:[1,0]
	v_pk_mul_f32 v[50:51], v[50:51], v[0:1] op_sel_hi:[1,0]
	v_pk_mul_f32 v[66:67], v[10:11], v[0:1] op_sel_hi:[1,0]
	v_pk_mul_f32 v[48:49], v[48:49], v[0:1] op_sel_hi:[1,0]
	ds_read2st64_b32 v[0:1], v4 offset1:1
	ds_read2st64_b32 v[2:3], v4 offset0:2 offset1:3
	ds_read2st64_b32 v[6:7], v4 offset0:4 offset1:5
	ds_read2st64_b32 v[8:9], v4 offset0:6 offset1:7
	v_pk_mul_f32 v[56:57], v[54:55], v[44:45]
	v_pk_mul_f32 v[64:65], v[50:51], v[42:43]
	v_cmp_lt_i32_e32 vcc, 0, v60
	s_waitcnt lgkmcnt(3)
	v_add_f32_e32 v0, v5, v0
	v_add_f32_e32 v1, v5, v1
	ds_write2st64_b32 v4, v0, v1 offset1:1
	s_waitcnt lgkmcnt(3)
	v_add_f32_e32 v0, v5, v2
	v_add_f32_e32 v1, v5, v3
	ds_write2st64_b32 v4, v0, v1 offset0:2 offset1:3
	s_waitcnt lgkmcnt(3)
	v_add_f32_e32 v0, v5, v6
	v_add_f32_e32 v1, v5, v7
	ds_write2st64_b32 v4, v0, v1 offset0:4 offset1:5
	s_waitcnt lgkmcnt(3)
	v_add_f32_e32 v0, v5, v8
	v_add_f32_e32 v1, v5, v9
	ds_write2st64_b32 v4, v0, v1 offset0:6 offset1:7
	v_max_i32_e32 v0, 1, v60
	v_lshl_add_u32 v0, v0, 8, s77
	v_lshlrev_b32_e32 v1, 2, v52
	s_waitcnt lgkmcnt(0)
	s_barrier
	v_add3_u32 v0, v0, v1, s0
	ds_read_b128 v[8:11], v62
	ds_read_b128 v[20:23], v62 offset:16
	ds_read_b128 v[24:27], v0
	ds_read_b128 v[42:45], v0 offset:16
	v_add_u32_e32 v0, 0, v1
	v_add_u32_e32 v0, 0x21300, v0
	ds_read_b128 v[4:7], v0
	ds_read_b128 v[0:3], v0 offset:16
	v_cndmask_b32_e64 v80, 0, 1.0, vcc
	s_waitcnt lgkmcnt(3)
	v_mul_f32_e32 v63, v80, v24
	v_mul_f32_e32 v24, 0x3fb8aa3b, v8
	v_mul_f32_e32 v62, 0xbfb8aa3b, v8
	s_waitcnt lgkmcnt(1)
	v_sub_f32_e32 v8, v4, v8
	v_mul_f32_e32 v8, 0x3fb8aa3b, v8
	v_exp_f32_e32 v8, v8
	v_mul_f32_e32 v63, 0x3fb8aa3b, v63
	v_exp_f32_e32 v70, v63
	v_mul_f32_e32 v63, 0xbfb8aa3b, v9
	v_mul_f32_e32 v81, v56, v8
	v_mul_f32_e32 v82, v14, v8
	v_mul_f32_e32 v8, v80, v25
	v_mul_f32_e32 v8, 0x3fb8aa3b, v8
	v_exp_f32_e32 v71, v8
	v_sub_f32_e32 v8, v5, v9
	v_mul_f32_e32 v25, 0x3fb8aa3b, v9
	v_mul_f32_e32 v8, 0x3fb8aa3b, v8
	v_exp_f32_e32 v24, v24
	v_exp_f32_e32 v62, v62
	v_exp_f32_e32 v25, v25
	v_exp_f32_e32 v63, v63
	v_exp_f32_e32 v8, v8
	v_mul_f32_e32 v9, v80, v26
	v_pk_mul_f32 v[12:13], v[12:13], v[24:25]
	v_pk_mul_f32 v[24:25], v[56:57], v[62:63]
	v_pk_mul_f32 v[62:63], v[14:15], v[62:63]
	v_mul_f32_e32 v56, v57, v8
	v_mul_f32_e32 v57, v15, v8
	v_mul_f32_e32 v8, 0x3fb8aa3b, v10
	v_mul_f32_e32 v14, 0xbfb8aa3b, v10
	v_sub_f32_e32 v10, v6, v10
	v_mul_f32_e32 v10, 0x3fb8aa3b, v10
	v_exp_f32_e32 v10, v10
	v_pk_mul_f32 v[54:55], v[70:71], v[54:55] neg_lo:[0,1] neg_hi:[0,1]
	v_mul_f32_e32 v9, 0x3fb8aa3b, v9
	v_exp_f32_e32 v26, v9
	v_mul_f32_e32 v70, v64, v10
	v_mul_f32_e32 v71, v28, v10
	v_mul_f32_e32 v10, v80, v27
	v_mul_f32_e32 v9, 0x3fb8aa3b, v11
	v_mul_f32_e32 v15, 0xbfb8aa3b, v11
	v_mul_f32_e32 v10, 0x3fb8aa3b, v10
	v_exp_f32_e32 v8, v8
	v_exp_f32_e32 v14, v14
	v_exp_f32_e32 v9, v9
	v_exp_f32_e32 v15, v15
	v_exp_f32_e32 v27, v10
	v_sub_f32_e32 v10, v7, v11
	v_mul_f32_e32 v10, 0x3fb8aa3b, v10
	v_exp_f32_e32 v83, v10
	v_pk_mul_f32 v[50:51], v[26:27], v[50:51] neg_lo:[0,1] neg_hi:[0,1]
	v_pk_mul_f32 v[10:11], v[36:37], v[8:9]
	v_pk_mul_f32 v[26:27], v[64:65], v[14:15]
	v_pk_mul_f32 v[14:15], v[28:29], v[14:15]
	v_mul_f32_e32 v8, 0x3fb8aa3b, v20
	v_mul_f32_e32 v28, 0xbfb8aa3b, v20
	s_waitcnt lgkmcnt(0)
; __device__ __forceinline__ unsigned pk2(float lo, float hi) { const f32x2h v = {lo, hi}; const bf16x2h b = __builtin_convertvector(v, bf16x2h); return __builtin_bit_cast(unsigned, b); }
; __device__ __forceinline__ bf16 f2bf(float f) { return (bf16)(pk2(f, f) & 0xffffu); }
; __device__ __forceinline__ void phase1(const int WID_, const In& I, char* lds) {
;     ...
;             for (int e = 0; e < 8; ++e) { const float g = gv_[e], gm1 = mv_[e] * msk, gL = lv_[e];
;                 glast[e] = gL;
;                 const float eg = __expf(g), eng = __expf(-g), egm = __expf(gm1), egl = __expf(gL - g);
;                 ab[e] = -kk_[e] * egm; rb[e] = r_[e] * eg; bb[e] = b_[e] * eng; kb[e] = kp_[e] * eng; bt[e] = b_[e] * egl; kt[e] = kp_[e] * egl; }
; #pragma unroll
;             for (int q = 0; q < 4; ++q) { pab[q] = pk2(ab[2 * q], ab[2 * q + 1]); prb[q] = pk2(rb[2 * q], rb[2 * q + 1]); pbb[q] = pk2(bb[2 * q], bb[2 * q + 1]); pkb[q] = pk2(kb[2 * q], kb[2 * q + 1]); }
;             *(uint4*)(MAT(O_AB) + s * LD + cg * 8) = make_uint4(pab[0], pab[1], pab[2], pab[3]);
;             *(uint4*)(MAT(O_RB) + s * LD + cg * 8) = make_uint4(prb[0], prb[1], prb[2], prb[3]);
;             *(uint4*)(MAT(O_BB) + s * LD + cg * 8) = make_uint4(pbb[0], pbb[1], pbb[2], pbb[3]);
;             *(uint4*)(MAT(O_KB) + s * LD + cg * 8) = make_uint4(pkb[0], pkb[1], pkb[2], pkb[3]);
; #pragma unroll
;             for (int e = 0; e < 8; ++e) { const int k = cg * 8 + e;
;                 MAT(O_AT)[k * LD + s] = f2bf(ab[e]); MAT(O_BT)[k * LD + s] = f2bf(bt[e]); MAT(O_KT)[k * LD + s] = f2bf(kt[e]); MAT(O_VT)[k * LD + s] = f2bf(v_[e]); }
	v_sub_f32_e32 v20, v0, v20
	v_mul_f32_e32 v20, 0x3fb8aa3b, v20
	v_exp_f32_e32 v20, v20
	v_pk_mul_f32 v[46:47], v[66:67], v[46:47]
	v_mul_f32_e32 v64, v65, v83
	v_mul_f32_e32 v65, v29, v83
	v_mul_f32_e32 v83, v46, v20
	v_mul_f32_e32 v84, v40, v20
	v_mul_f32_e32 v20, v80, v43
	v_mul_f32_e32 v9, v80, v42
	v_mul_f32_e32 v20, 0x3fb8aa3b, v20
	v_mul_f32_e32 v9, 0x3fb8aa3b, v9
	v_exp_f32_e32 v37, v20
	v_sub_f32_e32 v20, v1, v21
	v_exp_f32_e32 v36, v9
	v_mul_f32_e32 v9, 0x3fb8aa3b, v21
	v_mul_f32_e32 v29, 0xbfb8aa3b, v21
	v_mul_f32_e32 v20, 0x3fb8aa3b, v20
	v_sub_f32_e32 v21, v2, v22
	v_exp_f32_e32 v8, v8
	v_exp_f32_e32 v9, v9
	v_exp_f32_e32 v20, v20
	v_mul_f32_e32 v21, 0x3fb8aa3b, v21
	v_exp_f32_e32 v21, v21
	v_exp_f32_e32 v28, v28
	v_exp_f32_e32 v29, v29
	v_pk_mul_f32 v[34:35], v[48:49], v[34:35]
	v_pk_mul_f32 v[36:37], v[36:37], v[66:67] neg_lo:[0,1] neg_hi:[0,1]
	v_pk_mul_f32 v[32:33], v[32:33], v[8:9]
	v_mul_f32_e32 v66, v47, v20
	v_mul_f32_e32 v67, v41, v20
	v_mul_f32_e32 v9, v80, v44
	v_mul_f32_e32 v8, 0x3fb8aa3b, v22
	v_mul_f32_e32 v20, 0xbfb8aa3b, v22
	v_mul_f32_e32 v22, v80, v45
	v_mul_f32_e32 v9, 0x3fb8aa3b, v9
	v_mul_f32_e32 v85, v34, v21
	v_mul_f32_e32 v86, v30, v21
	v_mul_f32_e32 v21, 0xbfb8aa3b, v23
	v_mul_f32_e32 v22, 0x3fb8aa3b, v22
	v_pk_mul_f32 v[42:43], v[46:47], v[28:29]
	v_pk_mul_f32 v[28:29], v[40:41], v[28:29]
	v_exp_f32_e32 v20, v20
	v_exp_f32_e32 v40, v9
	v_mul_f32_e32 v9, 0x3fb8aa3b, v23
	v_exp_f32_e32 v21, v21
	v_exp_f32_e32 v41, v22
	v_sub_f32_e32 v22, v3, v23
	v_exp_f32_e32 v8, v8
	v_exp_f32_e32 v9, v9
	v_mul_f32_e32 v22, 0x3fb8aa3b, v22
	v_exp_f32_e32 v22, v22
	v_pk_mul_f32 v[40:41], v[40:41], v[48:49] neg_lo:[0,1] neg_hi:[0,1]
	v_pk_mul_f32 v[44:45], v[34:35], v[20:21]
	v_pk_mul_f32 v[46:47], v[30:31], v[20:21]
	v_cvt_pk_bf16_f32 v21, v26, v27
	v_cvt_pk_bf16_f32 v26, v28, v29
	v_mul_lo_u32 v28, v60, s9
	v_lshlrev_b32_e32 v29, 1, v52
	v_pk_mul_f32 v[38:39], v[38:39], v[8:9]
	v_cvt_pk_bf16_f32 v8, v54, v55
	v_cvt_pk_bf16_f32 v12, v12, v13
	v_cvt_pk_bf16_f32 v9, v50, v51
	v_cvt_pk_bf16_f32 v13, v10, v11
	v_cvt_pk_bf16_f32 v10, v36, v37
	v_cvt_pk_bf16_f32 v11, v40, v41
	v_add3_u32 v28, 0, v28, v29
	v_mul_f32_e32 v30, v35, v22
	v_mul_f32_e32 v31, v31, v22
	v_cvt_pk_bf16_f32 v20, v24, v25
	v_cvt_pk_bf16_f32 v24, v62, v63
	v_cvt_pk_bf16_f32 v25, v14, v15
	v_cvt_pk_bf16_f32 v14, v32, v33
	v_cvt_pk_bf16_f32 v22, v42, v43
	v_cvt_pk_bf16_f32 v15, v38, v39
	v_cvt_pk_bf16_f32 v23, v44, v45
	v_cvt_pk_bf16_f32 v27, v46, v47
	ds_write_b128 v28, v[8:11]
	ds_write_b128 v28, v[12:15] offset:9216
	ds_write_b128 v28, v[20:23] offset:18432
	ds_write_b128 v28, v[24:27] offset:27648
	v_and_b32_e32 v35, 2, v61
	v_cmp_ne_u32_e64 s[98:99], 0, v35
	v_bfe_i32 v35, v61, 0, 1
	v_bfe_i32 v38, v60, 0, 1
	v_and_b32_e32 v35, 0x2020202, v35
	v_and_b32_e32 v38, 0x6060606, v38
	v_xor_b32_e32 v32, 0x5040100, v35
	v_xor_b32_e32 v32, v32, v38
	v_and_b32_e32 v33, 3, v61
	v_xor_b32_e32 v33, v60, v33
	v_and_b32_e32 v33, 7, v33
	v_lshl_add_u32 v33, v61, 3, v33
	v_mul_u32_u24_e32 v33, 0x90, v33
	v_and_b32_e32 v34, -8, v60
	v_lshl_add_u32 v33, v34, 1, v33
	v_add_u32_e32 v34, 0x12000, v33
	v_cvt_pk_bf16_f32 v81, v81, v56
	v_cvt_pk_bf16_f32 v70, v70, v64
	v_cvt_pk_bf16_f32 v83, v83, v66
	v_cvt_pk_bf16_f32 v85, v85, v30
	v_cvt_pk_bf16_f32 v82, v82, v57
	v_cvt_pk_bf16_f32 v71, v71, v65
	v_cvt_pk_bf16_f32 v84, v84, v67
	v_cvt_pk_bf16_f32 v86, v86, v31
	v_cvt_pk_bf16_f32 v53, v53, v68
	v_cvt_pk_bf16_f32 v72, v72, v73
	v_cvt_pk_bf16_f32 v74, v74, v75
	v_cvt_pk_bf16_f32 v78, v78, v79
	v_mov_b32_dpp v55, v8 row_ror:8 row_mask:0xf bank_mask:0xf
	v_mov_b32_dpp v51, v9 row_ror:8 row_mask:0xf bank_mask:0xf
	v_mov_b32_dpp v37, v10 row_ror:8 row_mask:0xf bank_mask:0xf
	v_mov_b32_dpp v41, v11 row_ror:8 row_mask:0xf bank_mask:0xf
	v_mov_b32_dpp v56, v81 row_ror:8 row_mask:0xf bank_mask:0xf
	v_mov_b32_dpp v64, v70 row_ror:8 row_mask:0xf bank_mask:0xf
	v_mov_b32_dpp v66, v83 row_ror:8 row_mask:0xf bank_mask:0xf
	v_mov_b32_dpp v30, v85 row_ror:8 row_mask:0xf bank_mask:0xf
	v_mov_b32_dpp v57, v82 row_ror:8 row_mask:0xf bank_mask:0xf
	v_mov_b32_dpp v65, v71 row_ror:8 row_mask:0xf bank_mask:0xf
	v_mov_b32_dpp v67, v84 row_ror:8 row_mask:0xf bank_mask:0xf
	v_mov_b32_dpp v31, v86 row_ror:8 row_mask:0xf bank_mask:0xf
	v_mov_b32_dpp v68, v53 row_ror:8 row_mask:0xf bank_mask:0xf
	v_mov_b32_dpp v73, v72 row_ror:8 row_mask:0xf bank_mask:0xf
	v_mov_b32_dpp v75, v74 row_ror:8 row_mask:0xf bank_mask:0xf
	v_mov_b32_dpp v79, v78 row_ror:8 row_mask:0xf bank_mask:0xf
	v_perm_b32 v54, v55, v8, v32
	v_perm_b32 v50, v51, v9, v32
	v_perm_b32 v36, v37, v10, v32
	v_perm_b32 v40, v41, v11, v32
	v_perm_b32 v81, v56, v81, v32
	v_perm_b32 v70, v64, v70, v32
	v_perm_b32 v83, v66, v83, v32
	v_perm_b32 v85, v30, v85, v32
	v_perm_b32 v82, v57, v82, v32
	v_perm_b32 v71, v65, v71, v32
	v_perm_b32 v84, v67, v84, v32
	v_perm_b32 v86, v31, v86, v32
	v_perm_b32 v53, v68, v53, v32
	v_perm_b32 v72, v73, v72, v32
	v_perm_b32 v74, v75, v74, v32
	v_perm_b32 v78, v79, v78, v32
	v_cndmask_b32_e64 v8, v54, v50, s[98:99]
	v_cndmask_b32_e64 v9, v50, v54, s[98:99]
	v_cndmask_b32_e64 v10, v36, v40, s[98:99]
	v_cndmask_b32_e64 v11, v40, v36, s[98:99]
	v_cndmask_b32_e64 v12, v81, v70, s[98:99]
	v_cndmask_b32_e64 v13, v70, v81, s[98:99]
	v_cndmask_b32_e64 v14, v83, v85, s[98:99]
	v_cndmask_b32_e64 v15, v85, v83, s[98:99]
	v_cndmask_b32_e64 v20, v82, v71, s[98:99]
	v_cndmask_b32_e64 v21, v71, v82, s[98:99]
	v_cndmask_b32_e64 v22, v84, v86, s[98:99]
	v_cndmask_b32_e64 v23, v86, v84, s[98:99]
	v_cndmask_b32_e64 v24, v53, v72, s[98:99]
	v_cndmask_b32_e64 v25, v72, v53, s[98:99]
	v_cndmask_b32_e64 v26, v74, v78, s[98:99]
	v_cndmask_b32_e64 v27, v78, v74, s[98:99]
	v_permlane16_swap_b32_e32 v8, v9
	v_permlane16_swap_b32_e32 v10, v11
	v_permlane16_swap_b32_e32 v12, v13
	v_permlane16_swap_b32_e32 v14, v15
	v_permlane16_swap_b32_e32 v20, v21
	v_permlane16_swap_b32_e32 v22, v23
	v_permlane16_swap_b32_e32 v24, v25
	v_permlane16_swap_b32_e32 v26, v27
	v_permlane32_swap_b32_e32 v8, v10
	v_permlane32_swap_b32_e32 v9, v11
	v_permlane32_swap_b32_e32 v12, v14
	v_permlane32_swap_b32_e32 v13, v15
	v_permlane32_swap_b32_e32 v20, v22
	v_permlane32_swap_b32_e32 v21, v23
	v_permlane32_swap_b32_e32 v24, v26
	v_permlane32_swap_b32_e32 v25, v27
	s_nop 1
	ds_write_b128 v33, v[8:11] offset:36864
	ds_write_b128 v33, v[12:15] offset:55296
	ds_write_b128 v33, v[20:23] offset:64512
	ds_write_b128 v34, v[24:27]
	s_waitcnt lgkmcnt(0)
	s_barrier
; __device__ __forceinline__ void phase1(const int WID_, const In& I, char* lds) {
;     ...
;         P1_LOADS(item + GN);
;         if (s == 63) {
; #pragma unroll
;             for (int e = 0; e < 8; ++e) TOT[cg * 8 + e] = __expf(glast[e]);
;         }
	v_mbcnt_lo_u32_b32 v8, -1, 0
	v_mbcnt_hi_u32_b32 v8, -1, v8
	s_ashr_i32 s0, s1, 10
	v_add_u32_e32 v9, s86, v8
	s_lshr_b32 s4, s1, 1
	s_lshl_b32 s1, s1, 6
	v_ashrrev_i32_e32 v9, 3, v9
	s_and_b32 s4, s4, 0x1c0
	v_lshlrev_b32_e32 v8, 3, v8
	s_and_b32 s1, s1, 0x1fc0
	v_and_or_b32 v14, v8, 56, s4
	v_add_u32_e32 v8, s1, v9
	s_ashr_i32 s1, s0, 31
	s_lshl_b64 s[0:1], s[0:1], 13
	v_ashrrev_i32_e32 v9, 31, v8
	v_lshl_add_u64 v[10:11], s[0:1], 0, v[8:9]
	v_mov_b64_e32 v[12:13], s[92:93]
	v_mad_u64_u32 v[12:13], s[0:1], v10, s8, v[12:13]
	v_mad_i32_i24 v13, v11, s8, v13
	v_lshlrev_b32_e32 v68, 1, v14
	v_cmp_lt_i32_e32 vcc, 0, v8
	v_lshl_add_u64 v[12:13], v[12:13], 0, v[68:69]
	v_readlane_b32 s0, v242, 37
	v_cndmask_b32_e64 v9, 0, -1, vcc
	v_cndmask_b32_e32 v8, 0, v76, vcc
	v_lshl_add_u64 v[8:9], v[12:13], 0, v[8:9]
	global_load_dwordx4 v[36:39], v[12:13], off
	global_load_dwordx4 v[28:31], v[12:13], off offset:1024
	global_load_dwordx4 v[20:23], v[12:13], off offset:2048
	global_load_dwordx4 v[44:47], v[8:9], off
	global_load_dwordx4 v[48:51], v[8:9], off offset:1024
	global_load_dwordx4 v[24:27], v[8:9], off offset:2048
	v_lshlrev_b64 v[8:9], 10, v[10:11]
	v_readlane_b32 s1, v242, 38
	v_cmp_eq_u32_e32 vcc, 63, v60
	s_nop 0
	v_lshl_add_u64 v[10:11], s[0:1], 0, v[8:9]
	v_lshl_add_u64 v[10:11], v[10:11], 0, v[68:69]
	v_lshl_add_u64 v[8:9], s[28:29], 0, v[8:9]
	v_lshl_add_u64 v[8:9], v[8:9], 0, v[68:69]
	global_load_dwordx4 v[32:35], v[10:11], off
	global_load_dwordx4 v[40:43], v[8:9], off
	s_and_saveexec_b64 s[0:1], vcc
	s_cbranch_execz .LBB0_1428
	v_mul_f32_e32 v4, 0x3fb8aa3b, v4
	v_mul_f32_e32 v5, 0x3fb8aa3b, v5
	v_mul_f32_e32 v6, 0x3fb8aa3b, v6
	v_mul_f32_e32 v7, 0x3fb8aa3b, v7
	v_exp_f32_e32 v4, v4
	v_exp_f32_e32 v5, v5
	v_exp_f32_e32 v6, v6
	v_exp_f32_e32 v7, v7
	v_mul_f32_e32 v0, 0x3fb8aa3b, v0
	v_mul_f32_e32 v1, 0x3fb8aa3b, v1
	v_mul_f32_e32 v2, 0x3fb8aa3b, v2
	v_mul_f32_e32 v3, 0x3fb8aa3b, v3
	v_exp_f32_e32 v0, v0
	v_exp_f32_e32 v1, v1
	v_exp_f32_e32 v2, v2
	v_exp_f32_e32 v3, v3
	v_lshl_add_u32 v8, v52, 2, 0
	v_add_u32_e32 v8, 0x21400, v8
	ds_write_b128 v8, v[4:7]
	ds_write_b128 v8, v[0:3] offset:16
